# speedup vs baseline: 1.0046x; 1.0032x over previous
.Lagg_loop:
	s_waitcnt vmcnt(4)
	s_mov_b32 s24, s0
	s_min_i32 s24, s24, s20
	s_mul_i32 s24, s24, s44
	s_add_i32 s24, s24, s45
	s_lshl_b32 s24, s24, 4
	v_add_u32_e32 v33, s24, v18
	v_cmp_gt_i32_e64 s[28:29], s17, v33
	s_add_i32 s24, s0, 16
	s_min_i32 s24, s24, s20
	s_mul_i32 s24, s24, s44
	s_add_i32 s24, s24, s45
	s_lshl_b32 s24, s24, 4
	s_ashr_i32 s25, s24, 31
	v_cndmask_b32_e64 v31, v59, v30, s[28:29]
	v_lshl_add_u64 v[32:33], s[24:25], 2, v[20:21]
	global_load_dword v30, v[32:33], off
	s_waitcnt vmcnt(4)
	s_movk_i32 s50, 0x140
	v_lshrrev_b32_e32 v32, 17, v29
	v_mad_u32_u24 v32, v32, s50, v23
	v_fma_mix_f32 v33, v2, v22, s23 op_sel_hi:[1,0,0]
	v_fma_mix_f32 v34, v2, v22, s23 op_sel:[1,0,0] op_sel_hi:[1,0,0]
	v_fma_mix_f32 v36, v3, v22, s23 op_sel_hi:[1,0,0]
	v_fma_mix_f32 v37, v3, v22, s23 op_sel:[1,0,0] op_sel_hi:[1,0,0]
	v_lshl_add_u32 v33, v34, 16, v33
	ds_add_u32 v32, v33
	v_fma_mix_f32 v33, v4, v22, s23 op_sel_hi:[1,0,0]
	v_fma_mix_f32 v34, v4, v22, s23 op_sel:[1,0,0] op_sel_hi:[1,0,0]
	v_lshl_add_u32 v36, v37, 16, v36
	ds_add_u32 v32, v36 offset:64
	v_fma_mix_f32 v36, v5, v22, s23 op_sel_hi:[1,0,0]
	v_fma_mix_f32 v37, v5, v22, s23 op_sel:[1,0,0] op_sel_hi:[1,0,0]
	v_lshl_add_u32 v33, v34, 16, v33
	ds_add_u32 v32, v33 offset:128
	s_nop 0
	v_lshl_add_u32 v36, v37, 16, v36
	ds_add_u32 v32, v36 offset:192
	v_mov_b32_e32 v29, 0
	s_nop 1
	v_mov_b32_dpp v29, v31 row_newbcast:0 row_mask:0xf bank_mask:0xf
	v_lshlrev_b32_e32 v35, 8, v29
	v_and_or_b32 v35, v35, s22, v24
	s_waitcnt vmcnt(2)
	global_load_dwordx4 v[2:5], v35, s[12:13]
	s_waitcnt vmcnt(4)
	s_movk_i32 s50, 0x140
	v_lshrrev_b32_e32 v32, 17, v27
	v_mad_u32_u24 v32, v32, s50, v23
	v_fma_mix_f32 v33, v6, v22, s23 op_sel_hi:[1,0,0]
	v_fma_mix_f32 v34, v6, v22, s23 op_sel:[1,0,0] op_sel_hi:[1,0,0]
	v_fma_mix_f32 v36, v7, v22, s23 op_sel_hi:[1,0,0]
	v_fma_mix_f32 v37, v7, v22, s23 op_sel:[1,0,0] op_sel_hi:[1,0,0]
	v_lshl_add_u32 v33, v34, 16, v33
	ds_add_u32 v32, v33
	v_fma_mix_f32 v33, v8, v22, s23 op_sel_hi:[1,0,0]
	v_fma_mix_f32 v34, v8, v22, s23 op_sel:[1,0,0] op_sel_hi:[1,0,0]
	v_lshl_add_u32 v36, v37, 16, v36
	ds_add_u32 v32, v36 offset:64
	v_fma_mix_f32 v36, v9, v22, s23 op_sel_hi:[1,0,0]
	v_fma_mix_f32 v37, v9, v22, s23 op_sel:[1,0,0] op_sel_hi:[1,0,0]
	v_lshl_add_u32 v33, v34, 16, v33
	ds_add_u32 v32, v33 offset:128
	s_nop 0
	v_lshl_add_u32 v36, v37, 16, v36
	ds_add_u32 v32, v36 offset:192
	v_mov_b32_e32 v27, 0
	s_nop 1
	v_mov_b32_dpp v27, v31 row_newbcast:1 row_mask:0xf bank_mask:0xf
	v_lshlrev_b32_e32 v35, 8, v27
	v_and_or_b32 v35, v35, s22, v24
	s_waitcnt vmcnt(1)
	global_load_dwordx4 v[6:9], v35, s[12:13]
	s_waitcnt vmcnt(4)
	s_movk_i32 s50, 0x140
	v_lshrrev_b32_e32 v32, 17, v28
	v_mad_u32_u24 v32, v32, s50, v23
	v_fma_mix_f32 v33, v10, v22, s23 op_sel_hi:[1,0,0]
	v_fma_mix_f32 v34, v10, v22, s23 op_sel:[1,0,0] op_sel_hi:[1,0,0]
	v_fma_mix_f32 v36, v11, v22, s23 op_sel_hi:[1,0,0]
	v_fma_mix_f32 v37, v11, v22, s23 op_sel:[1,0,0] op_sel_hi:[1,0,0]
	v_lshl_add_u32 v33, v34, 16, v33
	ds_add_u32 v32, v33
	v_fma_mix_f32 v33, v12, v22, s23 op_sel_hi:[1,0,0]
	v_fma_mix_f32 v34, v12, v22, s23 op_sel:[1,0,0] op_sel_hi:[1,0,0]
	v_lshl_add_u32 v36, v37, 16, v36
	ds_add_u32 v32, v36 offset:64
	v_fma_mix_f32 v36, v13, v22, s23 op_sel_hi:[1,0,0]
	v_fma_mix_f32 v37, v13, v22, s23 op_sel:[1,0,0] op_sel_hi:[1,0,0]
	v_lshl_add_u32 v33, v34, 16, v33
	ds_add_u32 v32, v33 offset:128
	s_nop 0
	v_lshl_add_u32 v36, v37, 16, v36
	ds_add_u32 v32, v36 offset:192
	v_mov_b32_e32 v28, 0
	s_nop 1
	v_mov_b32_dpp v28, v31 row_newbcast:2 row_mask:0xf bank_mask:0xf
	v_lshlrev_b32_e32 v35, 8, v28
	v_and_or_b32 v35, v35, s22, v24
	s_waitcnt vmcnt(1)
	global_load_dwordx4 v[10:13], v35, s[12:13]
	s_waitcnt vmcnt(4)
	s_movk_i32 s50, 0x140
	v_lshrrev_b32_e32 v32, 17, v26
	v_mad_u32_u24 v32, v32, s50, v23
	v_fma_mix_f32 v33, v14, v22, s23 op_sel_hi:[1,0,0]
	v_fma_mix_f32 v34, v14, v22, s23 op_sel:[1,0,0] op_sel_hi:[1,0,0]
	v_fma_mix_f32 v36, v15, v22, s23 op_sel_hi:[1,0,0]
	v_fma_mix_f32 v37, v15, v22, s23 op_sel:[1,0,0] op_sel_hi:[1,0,0]
	v_lshl_add_u32 v33, v34, 16, v33
	ds_add_u32 v32, v33
	v_fma_mix_f32 v33, v16, v22, s23 op_sel_hi:[1,0,0]
	v_fma_mix_f32 v34, v16, v22, s23 op_sel:[1,0,0] op_sel_hi:[1,0,0]
	v_lshl_add_u32 v36, v37, 16, v36
	ds_add_u32 v32, v36 offset:64
	v_fma_mix_f32 v36, v17, v22, s23 op_sel_hi:[1,0,0]
	v_fma_mix_f32 v37, v17, v22, s23 op_sel:[1,0,0] op_sel_hi:[1,0,0]
	v_lshl_add_u32 v33, v34, 16, v33
	ds_add_u32 v32, v33 offset:128
	s_nop 0
	v_lshl_add_u32 v36, v37, 16, v36
	ds_add_u32 v32, v36 offset:192
	v_mov_b32_e32 v26, 0
	s_nop 1
	v_mov_b32_dpp v26, v31 row_newbcast:3 row_mask:0xf bank_mask:0xf
	v_lshlrev_b32_e32 v35, 8, v26
	v_and_or_b32 v35, v35, s22, v24
	s_waitcnt vmcnt(1)
	global_load_dwordx4 v[14:17], v35, s[12:13]
	s_add_i32 s1, s1, 1
	s_add_i32 s0, s0, 16
	s_cmp_lt_u32 s1, s21
	s_cbranch_scc1 .Lagg_loop
